# moe_find: serial LDS table walk replaced by one 32-lane table read + compare + popcount (5 sites incl. the GEMM stream's next-unit decode)
# baseline (speedup 1.0000x reference)
.LBB0_1203:
	s_xor_b64 s[6:7], s[2:3], -1
	s_mov_b64 s[2:3], -1
	s_and_b64 vcc, exec, s[6:7]
	s_cbranch_vccz .LBB0_1198
	s_lshl_b32 s2, s14, 3
	s_or_b32 s6, s2, s13
	s_lshl_b32 s2, s12, 2
	s_add_i32 s2, s2, 0
	s_add_i32 s3, s2, 0x21004
	s_add_i32 s2, s12, 1
	v_and_b32_e32 v2, 63, v0
	v_lshlrev_b32_e32 v2, 2, v2
	v_add_u32_e32 v2, 0x21004, v2
	ds_read_b32 v2, v2
	s_waitcnt lgkmcnt(0)
	v_cmp_ge_i32_e64 s[84:85], s6, v2
	s_bcnt1_i32_b32 s12, s84
	s_lshl_b32 s7, s12, 2
	s_add_i32 s7, s7, 0x21000
	s_cmp_lt_u32 s11, 20
	s_cselect_b64 s[2:3], -1, 0
	s_and_b64 s[14:15], s[4:5], s[2:3]
	s_and_saveexec_b64 s[2:3], s[14:15]
	s_cbranch_execz .LBB0_1197
	s_mul_i32 s13, s11, 12
	s_add_i32 s13, s13, 0
	s_add_i32 s13, s13, 0x21400
	v_mov_b32_e32 v2, s13
	v_mov_b32_e32 v5, s12
	ds_write_b32 v2, v5
	v_mov_b32_e32 v5, s7
	ds_read_b32 v6, v5
	s_waitcnt lgkmcnt(0)
	v_readfirstlane_b32 s7, v6
	s_sub_i32 s6, s6, s7
	s_lshl_b32 s6, s6, 8
	v_mov_b32_e32 v6, s6
	ds_write_b32 v2, v6 offset:4
	ds_read_b32 v5, v5 offset:132
	s_waitcnt lgkmcnt(0)
	v_readfirstlane_b32 s6, v5
	s_nop 1
	v_mov_b32_e32 v5, s6
	ds_write_b32 v2, v5 offset:8
	s_branch .LBB0_1197

.LBB0_1238:
	s_andn2_b64 vcc, exec, s[2:3]
	v_readfirstlane_b32 s17, v0
	s_cbranch_vccnz .LBB0_1243
	s_lshl_b32 s2, s8, 3
	s_add_i32 s3, 0, 0x21004
	s_add_i32 s4, 0, 0x21000
	s_or_b32 s8, s2, s7
	s_mov_b32 s5, 1
	v_and_b32_e32 v2, 63, v0
	v_lshlrev_b32_e32 v2, 2, v2
	v_add_u32_e32 v2, 0x21004, v2
	ds_read_b32 v2, v2
	s_waitcnt lgkmcnt(0)
	v_cmp_ge_i32_e64 s[84:85], s8, v2
	s_bcnt1_i32_b32 s17, s84
	s_lshl_b32 s2, s17, 2
	s_add_i32 s2, s2, 0x21000
	v_mov_b32_e32 v2, v0
	s_load_dwordx2 s[2:3], s[0:1], 0xd0
	v_ashrrev_i32_e32 v6, 31, v2
	v_lshrrev_b32_e32 v6, 26, v6
	s_waitcnt vmcnt(9)
	v_lshlrev_b32_e32 v5, 4, v2
	v_add_u32_e32 v6, v2, v6
	v_bfe_i32 v2, v2, 27, 1
	v_lshrrev_b32_e32 v2, 22, v2
	s_bfe_u32 s26, s6, 0x30006
	v_add_u32_e32 v2, v5, v2
	v_and_b32_e32 v2, 0xfffffc00, v2
	s_waitcnt lgkmcnt(0)
	s_add_u32 s6, s2, 0x5a982000
	v_sub_u32_e32 v2, v5, v2
	s_addc_u32 s7, s3, 0
	s_add_i32 s4, s17, s14
	v_lshrrev_b32_e32 v5, 4, v2
	s_ashr_i32 s5, s4, 31
	v_bitop3_b32 v2, v5, v2, 32 bitop3:0x6c
	s_lshl_b32 s9, s26, 18
	s_lshl_b64 s[4:5], s[4:5], 21
	v_ashrrev_i32_e32 v5, 31, v2
	s_add_u32 s2, s2, s4
	v_lshrrev_b32_e32 v5, 26, v5
	s_addc_u32 s3, s3, s5
	v_ashrrev_i32_e32 v6, 6, v6
	v_add_u32_e32 v5, v2, v5
	s_add_u32 s2, s2, s9
	v_ashrrev_i32_e32 v7, 6, v5
	v_lshlrev_b32_e32 v6, 5, v6
	v_and_b32_e32 v5, 0xc0, v5
	s_addc_u32 s3, s3, 0
	s_waitcnt vmcnt(8)
	v_and_b32_e32 v8, 32, v6
	v_sub_u32_e32 v2, v2, v5
	s_add_u32 s4, s2, 0x26a2000
	v_lshlrev_b32_e32 v5, 2, v7
	v_and_b32_e32 v6, 0xffffffc0, v6
	v_readlane_b32 s2, v254, 4
	v_ashrrev_i16_sdwa v2, v196, sext(v2) dst_sel:DWORD dst_unused:UNUSED_PAD src0_sel:DWORD src1_sel:BYTE_0
	v_bfe_i32 v2, v2, 0, 16
	v_add3_u32 v5, s2, v5, v6
	ds_read2st64_b32 v[6:7], v5 offset1:1
	v_add_lshl_u32 v2, v8, v2, 1
	s_addc_u32 s5, s3, 0
	s_mov_b32 s19, 1
	s_waitcnt lgkmcnt(0)
	v_lshl_add_u32 v182, v6, 10, v2
	v_lshl_add_u32 v183, v7, 10, v2
	ds_read2st64_b32 v[6:7], v5 offset0:2 offset1:3
	v_mov_b32_e32 v180, s8
	s_waitcnt lgkmcnt(0)
	v_lshl_add_u32 v185, v6, 10, v2
	v_lshl_add_u32 v186, v7, 10, v2
	s_branch .LBB0_1244

.LBB0_1254:
	s_mov_b32 s82, 0
	s_andn2_b64 vcc, exec, s[2:3]
	s_mov_b64 s[12:13], 0
	s_cbranch_vccz .LBB0_1259
	s_lshl_b32 s2, s35, 3
	s_or_b32 s24, s2, s34
	s_mov_b32 s4, s29
	s_mov_b32 s5, s28
	s_mov_b32 s3, s27
	v_and_b32_e32 v2, 63, v0
	v_lshlrev_b32_e32 v2, 2, v2
	v_add_u32_e32 v2, 0x21004, v2
	ds_read_b32 v2, v2
	s_waitcnt lgkmcnt(0)
	v_cmp_ge_i32_e64 s[84:85], s24, v2
	s_bcnt1_i32_b32 s17, s84
	s_lshl_b32 s2, s17, 2
	s_add_i32 s2, s2, 0x21000
	v_mov_b32_e32 v2, v0
	s_add_i32 s2, s17, s14
	v_ashrrev_i32_e32 v182, 31, v2
	v_lshrrev_b32_e32 v182, 26, v182
	v_lshlrev_b32_e32 v181, 4, v2
	v_add_u32_e32 v182, v2, v182
	v_bfe_i32 v2, v2, 27, 1
	v_lshrrev_b32_e32 v2, 22, v2
	v_add_u32_e32 v2, v181, v2
	v_and_b32_e32 v2, 0xfffffc00, v2
	s_bfe_u32 s25, s18, 0x30006
	v_sub_u32_e32 v2, v181, v2
	s_ashr_i32 s3, s2, 31
	v_lshrrev_b32_e32 v181, 4, v2
	s_lshl_b32 s4, s25, 18
	s_lshl_b64 s[2:3], s[2:3], 21
	v_bitop3_b32 v2, v181, v2, 32 bitop3:0x6c
	s_add_u32 s2, s22, s2
	v_ashrrev_i32_e32 v181, 31, v2
	s_addc_u32 s3, s23, s3
	v_lshrrev_b32_e32 v181, 26, v181
	s_add_u32 s4, s2, s4
	v_ashrrev_i32_e32 v182, 6, v182
	v_add_u32_e32 v181, v2, v181
	s_addc_u32 s5, s3, 0
	s_lshl_b32 s2, s19, 10
	v_ashrrev_i32_e32 v183, 6, v181
	v_lshlrev_b32_e32 v182, 5, v182
	v_and_b32_e32 v181, 0xc0, v181
	s_add_i32 s2, s2, 0
	v_and_b32_e32 v185, 32, v182
	v_sub_u32_e32 v2, v2, v181
	v_and_b32_e32 v181, 0xffffffc0, v182
	s_add_i32 s2, s2, 0x22000
	v_lshlrev_b32_e32 v182, 2, v183
	v_add3_u32 v181, s2, v181, v182
	ds_read2st64_b32 v[182:183], v181 offset1:1
	ds_read2st64_b32 v[192:193], v181 offset0:2 offset1:3
	v_ashrrev_i16_sdwa v2, v196, sext(v2) dst_sel:DWORD dst_unused:UNUSED_PAD src0_sel:DWORD src1_sel:BYTE_0
	v_bfe_i32 v2, v2, 0, 16
	v_add_lshl_u32 v2, v185, v2, 1
	s_waitcnt lgkmcnt(0)
	v_lshl_add_u32 v182, v182, 10, v2
	v_lshl_add_u32 v183, v183, 10, v2
	v_lshl_add_u32 v185, v192, 10, v2
	v_lshl_add_u32 v186, v193, 10, v2
	s_add_i32 s19, s19, 1
	s_mov_b64 s[12:13], -1
	s_mov_b64 s[6:7], s[8:9]
	s_mov_b32 s18, s33

.LBB0_1377:
	s_andn2_b64 vcc, exec, s[2:3]
	v_readfirstlane_b32 s15, v0
	s_cbranch_vccnz .LBB0_1382
	s_lshl_b32 s2, s10, 3
	s_add_i32 s3, 0, 0x21004
	s_add_i32 s4, 0, 0x21000
	s_or_b32 s9, s2, s7
	s_mov_b32 s5, 1
	v_and_b32_e32 v2, 63, v0
	v_lshlrev_b32_e32 v2, 2, v2
	v_add_u32_e32 v2, 0x21004, v2
	ds_read_b32 v2, v2
	s_waitcnt lgkmcnt(0)
	v_cmp_ge_i32_e64 s[84:85], s9, v2
	s_bcnt1_i32_b32 s15, s84
	s_lshl_b32 s2, s15, 2
	s_add_i32 s2, s2, 0x21000
	v_mov_b32_e32 v2, v0
	s_load_dwordx2 s[2:3], s[0:1], 0xd0
	v_ashrrev_i32_e32 v6, 31, v2
	v_lshrrev_b32_e32 v6, 26, v6
	v_lshlrev_b32_e32 v5, 4, v2
	v_add_u32_e32 v6, v2, v6
	v_bfe_i32 v2, v2, 27, 1
	v_lshrrev_b32_e32 v2, 22, v2
	v_add_u32_e32 v2, v5, v2
	s_bfe_u32 s8, s6, 0x20006
	v_and_b32_e32 v2, 0xfffffc00, v2
	v_sub_u32_e32 v2, v5, v2
	s_waitcnt lgkmcnt(0)
	s_add_u32 s4, s2, 0x52182000
	v_readlane_b32 s6, v254, 7
	v_lshrrev_b32_e32 v5, 4, v2
	s_addc_u32 s5, s3, 0
	s_lshl_b32 s6, s6, 5
	v_bitop3_b32 v2, v5, v2, 32 bitop3:0x6c
	v_readlane_b32 s7, v254, 8
	s_add_i32 s6, s15, s6
	v_ashrrev_i32_e32 v7, 31, v2
	s_ashr_i32 s7, s6, 31
	v_lshrrev_b32_e32 v7, 26, v7
	s_lshl_b32 s10, s8, 18
	s_lshl_b64 s[6:7], s[6:7], 20
	v_add_u32_e32 v7, v2, v7
	s_add_u32 s2, s2, s6
	v_lshrrev_b32_e32 v8, 6, v7
	v_and_b32_e32 v7, 0xc0, v7
	s_addc_u32 s3, s3, s7
	v_ashrrev_i32_e32 v6, 6, v6
	v_sub_u32_e32 v2, v2, v7
	s_add_u32 s2, s2, s10
	v_lshlrev_b32_e32 v5, 3, v6
	v_lshlrev_b32_e32 v6, 5, v6
	v_ashrrev_i16_sdwa v2, v196, sext(v2) dst_sel:DWORD dst_unused:UNUSED_PAD src0_sel:DWORD src1_sel:BYTE_0
	s_addc_u32 s3, s3, 0
	v_and_b32_e32 v5, 0x3ffff0, v5
	v_and_b32_e32 v6, 32, v6
	v_bfe_i32 v2, v2, 0, 16
	s_add_u32 s6, s2, 0x126a2000
	s_addc_u32 s7, s3, 0
	s_lshl_b32 s2, s9, 18
	v_add_lshl_u32 v5, v8, v5, 10
	v_add_lshl_u32 v2, v6, v2, 1
	v_add3_u32 v182, v5, s2, v2
	s_mov_b32 s16, 1
	v_add_u32_e32 v183, 0x10000, v182
	v_add_u32_e32 v184, 0x20000, v182
	v_add_u32_e32 v185, 0x30000, v182
	v_mov_b32_e32 v180, s9
	v_mov_b32_e32 v220, s8
	s_branch .LBB0_1383

.LBB0_1393:
	s_mov_b32 s82, 0
	s_andn2_b64 vcc, exec, s[2:3]
	s_mov_b64 s[10:11], 0
	s_cbranch_vccz .LBB0_1398
	s_lshl_b32 s2, s27, 3
	s_or_b32 s18, s2, s26
	s_mov_b32 s4, s22
	s_mov_b32 s5, s21
	s_mov_b32 s3, s20
	v_and_b32_e32 v2, 63, v0
	v_lshlrev_b32_e32 v2, 2, v2
	v_add_u32_e32 v2, 0x21004, v2
	ds_read_b32 v2, v2
	s_waitcnt lgkmcnt(0)
	v_cmp_ge_i32_e64 s[84:85], s18, v2
	s_bcnt1_i32_b32 s15, s84
	s_lshl_b32 s2, s15, 2
	s_add_i32 s2, s2, 0x21000
	v_mov_b32_e32 v2, v0
	s_load_dwordx2 s[2:3], s[0:1], 0xd0
	v_ashrrev_i32_e32 v37, 31, v2
	v_lshrrev_b32_e32 v37, 26, v37
	v_lshlrev_b32_e32 v36, 4, v2
	v_add_u32_e32 v37, v2, v37
	v_bfe_i32 v2, v2, 27, 1
	v_lshrrev_b32_e32 v2, 22, v2
	v_add_u32_e32 v2, v36, v2
	v_and_b32_e32 v2, 0xfffffc00, v2
	s_bfe_u32 s19, s14, 0x20006
	s_add_i32 s16, s16, 1
	v_sub_u32_e32 v2, v36, v2
	v_lshrrev_b32_e32 v36, 4, v2
	s_waitcnt lgkmcnt(0)
	s_add_u32 s4, s2, 0x52182000
	v_bitop3_b32 v2, v36, v2, 32 bitop3:0x6c
	s_addc_u32 s5, s3, 0
	s_add_i32 s6, s15, s17
	v_ashrrev_i32_e32 v38, 31, v2
	s_ashr_i32 s7, s6, 31
	v_lshrrev_b32_e32 v38, 26, v38
	s_lshl_b32 s10, s19, 18
	s_lshl_b64 s[6:7], s[6:7], 20
	v_add_u32_e32 v38, v2, v38
	s_add_u32 s2, s2, s6
	v_lshrrev_b32_e32 v39, 6, v38
	v_and_b32_e32 v38, 0xc0, v38
	s_addc_u32 s3, s3, s7
	v_ashrrev_i32_e32 v37, 6, v37
	v_sub_u32_e32 v2, v2, v38
	s_add_u32 s2, s2, s10
	v_lshlrev_b32_e32 v36, 3, v37
	v_lshlrev_b32_e32 v37, 5, v37
	v_ashrrev_i16_sdwa v2, v196, sext(v2) dst_sel:DWORD dst_unused:UNUSED_PAD src0_sel:DWORD src1_sel:BYTE_0
	s_addc_u32 s3, s3, 0
	v_and_b32_e32 v36, 0x3ffff0, v36
	v_and_b32_e32 v37, 32, v37
	v_bfe_i32 v2, v2, 0, 16
	s_add_u32 s6, s2, 0x126a2000
	s_addc_u32 s7, s3, 0
	s_lshl_b32 s2, s18, 18
	v_add_lshl_u32 v36, v39, v36, 10
	v_add_lshl_u32 v2, v37, v2, 1
	v_add3_u32 v182, v36, s2, v2
	v_add_u32_e32 v183, 0x10000, v182
	v_add_u32_e32 v184, 0x20000, v182
	v_add_u32_e32 v185, 0x30000, v182
	s_mov_b64 s[10:11], -1
	s_mov_b32 s14, s25
